# mlstm Mrow prefix-max as DPP wave scan; conv_gate rewritten: 16 positions per lane, all rows loaded once with counted waits
# speedup vs baseline: 1.0040x; 1.0040x over previous
; __device__ __forceinline__ void mlstm_D(LAS unsigned char* lds, int c, int h, const bf16_t* Z, const float* gi, const float* bcum, const float* marr, const bf16_t* CST, const float* NST,
;                                         const float* hgain, bf16_t* YCAT) {
;     ...
;     const int t0 = c * CH; const float mc = marr[h * 65 + c];
;     __syncthreads();
;     if (tid < CH) gS[tid] = gi[(size_t)(t0 + tid) * 4 + h];
;     else if (tid < CH + DH) nst[tid - CH] = NST[(size_t)(c * NH + h) * DH + (tid - CH)];
;     __syncthreads();
;     if (tid < CH) { float m = mc; for (int s = 0; s <= tid; ++s) m = fmaxf(m, gS[s]); Mrow[tid] = m; }
.LBB0_564:
	s_or_b64 exec, exec, s[2:3]
	s_waitcnt lgkmcnt(0)
	s_barrier
	s_and_saveexec_b64 s[4:5], vcc
	s_cbranch_execz .LBB0_576
	v_and_b32_e32 v3, 63, v99
	v_lshl_add_u32 v2, v99, 2, s61
	v_lshl_add_u32 v3, v3, 2, s61
	ds_read_b32 v4, v2
	ds_read_b32 v5, v3
	s_waitcnt vmcnt(0) lgkmcnt(0)
	s_nop 1
	v_max_f32_dpp v4, v4, v4 row_shr:1 row_mask:0xf bank_mask:0xf
	v_max_f32_dpp v5, v5, v5 row_shr:1 row_mask:0xf bank_mask:0xf
	s_nop 1
	v_max_f32_dpp v4, v4, v4 row_shr:2 row_mask:0xf bank_mask:0xf
	v_max_f32_dpp v5, v5, v5 row_shr:2 row_mask:0xf bank_mask:0xf
	s_nop 1
	v_max_f32_dpp v4, v4, v4 row_shr:4 row_mask:0xf bank_mask:0xf
	v_max_f32_dpp v5, v5, v5 row_shr:4 row_mask:0xf bank_mask:0xf
	s_nop 1
	v_max_f32_dpp v4, v4, v4 row_shr:8 row_mask:0xf bank_mask:0xf
	v_max_f32_dpp v5, v5, v5 row_shr:8 row_mask:0xf bank_mask:0xf
	s_nop 1
	v_max_f32_dpp v4, v4, v4 row_bcast:15 row_mask:0xa bank_mask:0xf
	v_max_f32_dpp v5, v5, v5 row_bcast:15 row_mask:0xa bank_mask:0xf
	s_nop 1
	v_max_f32_dpp v4, v4, v4 row_bcast:31 row_mask:0xc bank_mask:0xf
	v_max_f32_dpp v5, v5, v5 row_bcast:31 row_mask:0xc bank_mask:0xf
	s_nop 1
	v_readlane_b32 s2, v5, 63
	v_readfirstlane_b32 s3, v95
	s_cmp_ge_u32 s15, 64
	s_cselect_b32 s2, s2, s3
	v_max_f32_e32 v4, s2, v4
	v_max_f32_e32 v4, v95, v4
	v_lshl_add_u32 v2, v99, 2, s62
	ds_write_b32 v2, v4

; __device__ __forceinline__ int fresh_tid() { int t = threadIdx.x; asm volatile("" : "+v"(t)); return t; }
; __device__ __forceinline__ int fresh_bx() { int t = blockIdx.x; asm volatile("" : "+s"(t)); return t; }
; __device__ __forceinline__ void conv_gate(const bf16_t* ZB, const bf16_t* ZC, const float* cw, bf16_t* Y, int G) {
;     const int gid = fresh_bx() * NTHR + fresh_tid(), NT = G * NTHR;
;     for (int it = gid; it < T * 256; it += NT) {
;         const int t = it >> 8, col = (it & 255) * 8; const size_t o = (size_t)t * D + col;
;         const u32x4 z0 = *(const u32x4*)(ZC + o), gb = *(const u32x4*)(ZB + o);
;         const u32x4 z1 = (t >= 1) ? *(const u32x4*)(ZC + o - D) : (u32x4){0u, 0u, 0u, 0u}, z2 = (t >= 2) ? *(const u32x4*)(ZC + o - 2 * D) : (u32x4){0u, 0u, 0u, 0u};
;         const f32x4 wa0 = *(const f32x4*)(cw + col), wa1 = *(const f32x4*)(cw + col + 4), wb0 = *(const f32x4*)(cw + D + col), wb1 = *(const f32x4*)(cw + D + col + 4),
;                     wc0 = *(const f32x4*)(cw + 2 * D + col), wc1 = *(const f32x4*)(cw + 2 * D + col + 4);
.LBB0_1599:
	s_waitcnt lgkmcnt(0)
	s_cmp_eq_u32 s19, 15
	s_cselect_b64 s[2:3], -1, 0
	s_or_b64 s[2:3], s[38:39], s[2:3]
	s_andn2_b64 vcc, exec, s[2:3]
	s_cbranch_vccnz .LBB0_1653
	s_mov_b32 s2, 0
	s_mov_b32 s2, s18
	s_load_dword s2, s[0:1], 0xf8
	s_mov_b64 s[10:11], s[0:1]
	s_mov_b32 s3, s18
	s_waitcnt vmcnt(0)
	v_mov_b32_e32 v2, v0
	s_add_u32 s4, s0, 0xf8
	s_waitcnt lgkmcnt(0)
	s_mov_b32 s22, s2
	s_mov_b32 s6, 0x200000
	v_lshl_add_u32 v1, s3, 9, v2
	s_addc_u32 s5, s1, 0
	v_cmp_gt_i32_e32 vcc, s6, v1
	s_and_saveexec_b64 s[6:7], vcc
	s_cbranch_execz .LBB0_1607
	s_load_dwordx2 s[14:15], s[10:11], 0xe0
	s_load_dwordx2 s[8:9], s[10:11], 0x70
	v_and_b32_e32 v1, 0xff, v0
	v_lshrrev_b32_e32 v2, 8, v0
	v_readfirstlane_b32 s26, v0
	v_lshlrev_b32_e32 v3, 4, v1
	v_lshlrev_b32_e32 v4, 5, v1
	s_lshl_b32 s12, s3, 5
	v_lshl_add_u32 v5, v2, 4, s12
	v_lshl_add_u32 v6, v5, 12, v3
	s_lshr_b32 s26, s26, 8
	s_or_b32 s26, s26, s3
	s_mov_b32 s27, 0xffff0000
	s_waitcnt lgkmcnt(0)
	s_add_u32 s10, s14, 0x3a800000
	s_addc_u32 s11, s15, 0
	s_add_u32 s12, s14, 0x3c800000
	s_addc_u32 s13, s15, 0
	s_add_u32 s14, s14, 0x40800000
	s_addc_u32 s15, s15, 0
	s_add_u32 s16, s8, 0x2000
	s_addc_u32 s17, s9, 0
	s_add_u32 s20, s8, 0x4000
	s_addc_u32 s21, s9, 0
	s_sub_u32 s24, s12, 0x2000
	s_subb_u32 s25, s13, 0
	global_load_dwordx4 v[8:11], v4, s[8:9]
	global_load_dwordx4 v[12:15], v4, s[8:9] offset:16
	global_load_dwordx4 v[16:19], v4, s[16:17]
	global_load_dwordx4 v[20:23], v4, s[16:17] offset:16
	global_load_dwordx4 v[24:27], v4, s[20:21]
	global_load_dwordx4 v[28:31], v4, s[20:21] offset:16
	global_load_dwordx4 v[76:79], v6, s[24:25]
	s_add_u32 s24, s24, 0x1000
	s_addc_u32 s25, s25, 0
	global_load_dwordx4 v[80:83], v6, s[24:25]
	global_load_dwordx4 v[84:87], v6, s[12:13]
	global_load_dwordx4 v[148:151], v6, s[10:11]
	s_add_u32 s12, s12, 0x1000
	s_addc_u32 s13, s13, 0
	s_add_u32 s10, s10, 0x1000
	s_addc_u32 s11, s11, 0
	global_load_dwordx4 v[88:91], v6, s[12:13]
	global_load_dwordx4 v[152:155], v6, s[10:11]
	s_add_u32 s12, s12, 0x1000
	s_addc_u32 s13, s13, 0
	s_add_u32 s10, s10, 0x1000
	s_addc_u32 s11, s11, 0
	global_load_dwordx4 v[92:95], v6, s[12:13]
	global_load_dwordx4 v[156:159], v6, s[10:11]
	s_add_u32 s12, s12, 0x1000
	s_addc_u32 s13, s13, 0
	s_add_u32 s10, s10, 0x1000
	s_addc_u32 s11, s11, 0
	global_load_dwordx4 v[96:99], v6, s[12:13]
	global_load_dwordx4 v[160:163], v6, s[10:11]
	s_add_u32 s12, s12, 0x1000
	s_addc_u32 s13, s13, 0
	s_add_u32 s10, s10, 0x1000
	s_addc_u32 s11, s11, 0
	global_load_dwordx4 v[100:103], v6, s[12:13]
	global_load_dwordx4 v[164:167], v6, s[10:11]
	s_add_u32 s12, s12, 0x1000
	s_addc_u32 s13, s13, 0
	s_add_u32 s10, s10, 0x1000
	s_addc_u32 s11, s11, 0
	global_load_dwordx4 v[104:107], v6, s[12:13]
	global_load_dwordx4 v[168:171], v6, s[10:11]
	s_add_u32 s12, s12, 0x1000
	s_addc_u32 s13, s13, 0
	s_add_u32 s10, s10, 0x1000
	s_addc_u32 s11, s11, 0
	global_load_dwordx4 v[108:111], v6, s[12:13]
	global_load_dwordx4 v[172:175], v6, s[10:11]
	s_add_u32 s12, s12, 0x1000
	s_addc_u32 s13, s13, 0
	s_add_u32 s10, s10, 0x1000
	s_addc_u32 s11, s11, 0
	global_load_dwordx4 v[112:115], v6, s[12:13]
	global_load_dwordx4 v[176:179], v6, s[10:11]
	s_add_u32 s12, s12, 0x1000
	s_addc_u32 s13, s13, 0
	s_add_u32 s10, s10, 0x1000
	s_addc_u32 s11, s11, 0
	global_load_dwordx4 v[116:119], v6, s[12:13]
	global_load_dwordx4 v[180:183], v6, s[10:11]
	s_add_u32 s12, s12, 0x1000
	s_addc_u32 s13, s13, 0
	s_add_u32 s10, s10, 0x1000
	s_addc_u32 s11, s11, 0
	global_load_dwordx4 v[120:123], v6, s[12:13]
	global_load_dwordx4 v[184:187], v6, s[10:11]
	s_add_u32 s12, s12, 0x1000
	s_addc_u32 s13, s13, 0
	s_add_u32 s10, s10, 0x1000
	s_addc_u32 s11, s11, 0
	global_load_dwordx4 v[124:127], v6, s[12:13]
	global_load_dwordx4 v[188:191], v6, s[10:11]
	s_add_u32 s12, s12, 0x1000
	s_addc_u32 s13, s13, 0
	s_add_u32 s10, s10, 0x1000
	s_addc_u32 s11, s11, 0
	global_load_dwordx4 v[128:131], v6, s[12:13]
	global_load_dwordx4 v[192:195], v6, s[10:11]
	s_add_u32 s12, s12, 0x1000
	s_addc_u32 s13, s13, 0
	s_add_u32 s10, s10, 0x1000
	s_addc_u32 s11, s11, 0
	global_load_dwordx4 v[132:135], v6, s[12:13]
	global_load_dwordx4 v[196:199], v6, s[10:11]
	s_add_u32 s12, s12, 0x1000
	s_addc_u32 s13, s13, 0
	s_add_u32 s10, s10, 0x1000
	s_addc_u32 s11, s11, 0
	global_load_dwordx4 v[136:139], v6, s[12:13]
	global_load_dwordx4 v[200:203], v6, s[10:11]
	s_add_u32 s12, s12, 0x1000
	s_addc_u32 s13, s13, 0
	s_add_u32 s10, s10, 0x1000
	s_addc_u32 s11, s11, 0
	global_load_dwordx4 v[140:143], v6, s[12:13]
	global_load_dwordx4 v[204:207], v6, s[10:11]
	s_add_u32 s12, s12, 0x1000
	s_addc_u32 s13, s13, 0
	s_add_u32 s10, s10, 0x1000
	s_addc_u32 s11, s11, 0
	global_load_dwordx4 v[144:147], v6, s[12:13]
	global_load_dwordx4 v[208:211], v6, s[10:11]
	s_waitcnt vmcnt(32)
	s_cmp_lg_u32 s26, 0
	s_cbranch_scc1 .Lcg2_in
	v_mov_b32_e32 v76, 0
	v_mov_b32_e32 v77, 0
	v_mov_b32_e32 v78, 0
	v_mov_b32_e32 v79, 0
	v_mov_b32_e32 v80, 0
	v_mov_b32_e32 v81, 0
	v_mov_b32_e32 v82, 0
	v_mov_b32_e32 v83, 0
; __device__ __forceinline__ unsigned cvt_pk_bf16(float lo, float hi) { unsigned r; asm volatile("v_cvt_pk_bf16_f32 %0, %1, %2" : "=v"(r) : "v"(lo), "v"(hi)); return r; }
; __device__ __forceinline__ int fresh_tid() { int t = threadIdx.x; asm volatile("" : "+v"(t)); return t; }
; __device__ __forceinline__ int fresh_bx() { int t = blockIdx.x; asm volatile("" : "+s"(t)); return t; }
; __device__ __forceinline__ void conv_gate(const bf16_t* ZB, const bf16_t* ZC, const float* cw, bf16_t* Y, int G) {
;     const int gid = fresh_bx() * NTHR + fresh_tid(), NT = G * NTHR;
;     for (int it = gid; it < T * 256; it += NT) {
;         const int t = it >> 8, col = (it & 255) * 8; const size_t o = (size_t)t * D + col;
;         const u32x4 z0 = *(const u32x4*)(ZC + o), gb = *(const u32x4*)(ZB + o);
;         const u32x4 z1 = (t >= 1) ? *(const u32x4*)(ZC + o - D) : (u32x4){0u, 0u, 0u, 0u}, z2 = (t >= 2) ? *(const u32x4*)(ZC + o - 2 * D) : (u32x4){0u, 0u, 0u, 0u};
;         const f32x4 wa0 = *(const f32x4*)(cw + col), wa1 = *(const f32x4*)(cw + col + 4), wb0 = *(const f32x4*)(cw + D + col), wb1 = *(const f32x4*)(cw + D + col + 4),
;                     wc0 = *(const f32x4*)(cw + 2 * D + col), wc1 = *(const f32x4*)(cw + 2 * D + col + 4);
;         float r[8];
;         r[0] = bf_lo(gb.x) * (wa0[0] * bf_lo(z2.x) + wb0[0] * bf_lo(z1.x) + wc0[0] * bf_lo(z0.x)); r[1] = bf_hi(gb.x) * (wa0[1] * bf_hi(z2.x) + wb0[1] * bf_hi(z1.x) + wc0[1] * bf_hi(z0.x));
;         r[2] = bf_lo(gb.y) * (wa0[2] * bf_lo(z2.y) + wb0[2] * bf_lo(z1.y) + wc0[2] * bf_lo(z0.y)); r[3] = bf_hi(gb.y) * (wa0[3] * bf_hi(z2.y) + wb0[3] * bf_hi(z1.y) + wc0[3] * bf_hi(z0.y));
;         r[4] = bf_lo(gb.z) * (wa1[0] * bf_lo(z2.z) + wb1[0] * bf_lo(z1.z) + wc1[0] * bf_lo(z0.z)); r[5] = bf_hi(gb.z) * (wa1[1] * bf_hi(z2.z) + wb1[1] * bf_hi(z1.z) + wc1[1] * bf_hi(z0.z));
;         r[6] = bf_lo(gb.w) * (wa1[2] * bf_lo(z2.w) + wb1[2] * bf_lo(z1.w) + wc1[2] * bf_lo(z0.w)); r[7] = bf_hi(gb.w) * (wa1[3] * bf_hi(z2.w) + wb1[3] * bf_hi(z1.w) + wc1[3] * bf_hi(z0.w));
;         u32x4 w; w.x = cvt_pk_bf16(r[0], r[1]); w.y = cvt_pk_bf16(r[2], r[3]); w.z = cvt_pk_bf16(r[4], r[5]); w.w = cvt_pk_bf16(r[6], r[7]);
;         *(u32x4*)(Y + o) = w;
;     }
; }
.Lcg2_in:
	v_lshlrev_b32_e32 v32, 16, v76
	v_and_b32_e32 v33, s27, v76
	v_lshlrev_b32_e32 v34, 16, v77
	v_and_b32_e32 v35, s27, v77
	v_lshlrev_b32_e32 v36, 16, v78
	v_and_b32_e32 v37, s27, v78
	v_lshlrev_b32_e32 v38, 16, v79
	v_and_b32_e32 v39, s27, v79
	v_lshlrev_b32_e32 v40, 16, v80
	v_and_b32_e32 v41, s27, v80
	v_lshlrev_b32_e32 v42, 16, v81
	v_and_b32_e32 v43, s27, v81
	v_lshlrev_b32_e32 v44, 16, v82
	v_and_b32_e32 v45, s27, v82
	v_lshlrev_b32_e32 v46, 16, v83
	v_and_b32_e32 v47, s27, v83
	s_waitcnt vmcnt(30)
	v_lshlrev_b32_e32 v48, 16, v84
	v_and_b32_e32 v49, s27, v84
	v_lshlrev_b32_e32 v50, 16, v85
	v_and_b32_e32 v51, s27, v85
	v_lshlrev_b32_e32 v52, 16, v86
	v_and_b32_e32 v53, s27, v86
	v_lshlrev_b32_e32 v54, 16, v87
	v_and_b32_e32 v55, s27, v87
	v_lshlrev_b32_e32 v56, 16, v148
	v_and_b32_e32 v57, s27, v148
	v_lshlrev_b32_e32 v58, 16, v149
	v_and_b32_e32 v59, s27, v149
	v_lshlrev_b32_e32 v60, 16, v150
	v_and_b32_e32 v61, s27, v150
	v_lshlrev_b32_e32 v62, 16, v151
	v_and_b32_e32 v63, s27, v151
	v_pk_mul_f32 v[64:65], v[8:9], v[32:33]
	v_pk_mul_f32 v[66:67], v[10:11], v[34:35]
	v_pk_mul_f32 v[68:69], v[12:13], v[36:37]
	v_pk_mul_f32 v[70:71], v[14:15], v[38:39]
	v_pk_fma_f32 v[64:65], v[16:17], v[40:41], v[64:65]
	v_pk_fma_f32 v[66:67], v[18:19], v[42:43], v[66:67]
	v_pk_fma_f32 v[68:69], v[20:21], v[44:45], v[68:69]
	v_pk_fma_f32 v[70:71], v[22:23], v[46:47], v[70:71]
	v_pk_fma_f32 v[64:65], v[24:25], v[48:49], v[64:65]
	v_pk_fma_f32 v[66:67], v[26:27], v[50:51], v[66:67]
	v_pk_fma_f32 v[68:69], v[28:29], v[52:53], v[68:69]
	v_pk_fma_f32 v[70:71], v[30:31], v[54:55], v[70:71]
	v_pk_mul_f32 v[64:65], v[64:65], v[56:57]
	v_pk_mul_f32 v[66:67], v[66:67], v[58:59]
	v_pk_mul_f32 v[68:69], v[68:69], v[60:61]
	v_pk_mul_f32 v[70:71], v[70:71], v[62:63]
	v_cvt_pk_bf16_f32 v72, v64, v65
	v_cvt_pk_bf16_f32 v73, v66, v67
	v_cvt_pk_bf16_f32 v74, v68, v69
	v_cvt_pk_bf16_f32 v75, v70, v71
	global_store_dwordx4 v6, v[72:75], s[14:15]
	s_add_u32 s14, s14, 0x1000
	s_addc_u32 s15, s15, 0
	s_waitcnt vmcnt(29)
	v_lshlrev_b32_e32 v32, 16, v88
	v_and_b32_e32 v33, s27, v88
	v_lshlrev_b32_e32 v34, 16, v89
	v_and_b32_e32 v35, s27, v89
	v_lshlrev_b32_e32 v36, 16, v90
	v_and_b32_e32 v37, s27, v90
	v_lshlrev_b32_e32 v38, 16, v91
	v_and_b32_e32 v39, s27, v91
	v_lshlrev_b32_e32 v56, 16, v152
	v_and_b32_e32 v57, s27, v152
	v_lshlrev_b32_e32 v58, 16, v153
	v_and_b32_e32 v59, s27, v153
	v_lshlrev_b32_e32 v60, 16, v154
	v_and_b32_e32 v61, s27, v154
	v_lshlrev_b32_e32 v62, 16, v155
	v_and_b32_e32 v63, s27, v155
	v_pk_mul_f32 v[64:65], v[8:9], v[40:41]
	v_pk_mul_f32 v[66:67], v[10:11], v[42:43]
	v_pk_mul_f32 v[68:69], v[12:13], v[44:45]
	v_pk_mul_f32 v[70:71], v[14:15], v[46:47]
	v_pk_fma_f32 v[64:65], v[16:17], v[48:49], v[64:65]
	v_pk_fma_f32 v[66:67], v[18:19], v[50:51], v[66:67]
	v_pk_fma_f32 v[68:69], v[20:21], v[52:53], v[68:69]
	v_pk_fma_f32 v[70:71], v[22:23], v[54:55], v[70:71]
	v_pk_fma_f32 v[64:65], v[24:25], v[32:33], v[64:65]
	v_pk_fma_f32 v[66:67], v[26:27], v[34:35], v[66:67]
	v_pk_fma_f32 v[68:69], v[28:29], v[36:37], v[68:69]
	v_pk_fma_f32 v[70:71], v[30:31], v[38:39], v[70:71]
	v_pk_mul_f32 v[64:65], v[64:65], v[56:57]
	v_pk_mul_f32 v[66:67], v[66:67], v[58:59]
	v_pk_mul_f32 v[68:69], v[68:69], v[60:61]
	v_pk_mul_f32 v[70:71], v[70:71], v[62:63]
	v_cvt_pk_bf16_f32 v72, v64, v65
	v_cvt_pk_bf16_f32 v73, v66, v67
	v_cvt_pk_bf16_f32 v74, v68, v69
	v_cvt_pk_bf16_f32 v75, v70, v71
	global_store_dwordx4 v6, v[72:75], s[14:15]
	s_add_u32 s14, s14, 0x1000
	s_addc_u32 s15, s15, 0
	s_waitcnt vmcnt(28)
	v_lshlrev_b32_e32 v40, 16, v92
	v_and_b32_e32 v41, s27, v92
	v_lshlrev_b32_e32 v42, 16, v93
	v_and_b32_e32 v43, s27, v93
	v_lshlrev_b32_e32 v44, 16, v94
	v_and_b32_e32 v45, s27, v94
	v_lshlrev_b32_e32 v46, 16, v95
	v_and_b32_e32 v47, s27, v95
	v_lshlrev_b32_e32 v56, 16, v156
	v_and_b32_e32 v57, s27, v156
	v_lshlrev_b32_e32 v58, 16, v157
	v_and_b32_e32 v59, s27, v157
	v_lshlrev_b32_e32 v60, 16, v158
	v_and_b32_e32 v61, s27, v158
	v_lshlrev_b32_e32 v62, 16, v159
	v_and_b32_e32 v63, s27, v159
	v_pk_mul_f32 v[64:65], v[8:9], v[48:49]
	v_pk_mul_f32 v[66:67], v[10:11], v[50:51]
	v_pk_mul_f32 v[68:69], v[12:13], v[52:53]
	v_pk_mul_f32 v[70:71], v[14:15], v[54:55]
	v_pk_fma_f32 v[64:65], v[16:17], v[32:33], v[64:65]
	v_pk_fma_f32 v[66:67], v[18:19], v[34:35], v[66:67]
	v_pk_fma_f32 v[68:69], v[20:21], v[36:37], v[68:69]
	v_pk_fma_f32 v[70:71], v[22:23], v[38:39], v[70:71]
	v_pk_fma_f32 v[64:65], v[24:25], v[40:41], v[64:65]
	v_pk_fma_f32 v[66:67], v[26:27], v[42:43], v[66:67]
	v_pk_fma_f32 v[68:69], v[28:29], v[44:45], v[68:69]
	v_pk_fma_f32 v[70:71], v[30:31], v[46:47], v[70:71]
	v_pk_mul_f32 v[64:65], v[64:65], v[56:57]
	v_pk_mul_f32 v[66:67], v[66:67], v[58:59]
	v_pk_mul_f32 v[68:69], v[68:69], v[60:61]
	v_pk_mul_f32 v[70:71], v[70:71], v[62:63]
	v_cvt_pk_bf16_f32 v72, v64, v65
	v_cvt_pk_bf16_f32 v73, v66, v67
	v_cvt_pk_bf16_f32 v74, v68, v69
	v_cvt_pk_bf16_f32 v75, v70, v71
	global_store_dwordx4 v6, v[72:75], s[14:15]
	s_add_u32 s14, s14, 0x1000
	s_addc_u32 s15, s15, 0
	s_waitcnt vmcnt(27)
; __device__ __forceinline__ unsigned cvt_pk_bf16(float lo, float hi) { unsigned r; asm volatile("v_cvt_pk_bf16_f32 %0, %1, %2" : "=v"(r) : "v"(lo), "v"(hi)); return r; }
; __device__ __forceinline__ int fresh_tid() { int t = threadIdx.x; asm volatile("" : "+v"(t)); return t; }
; __device__ __forceinline__ int fresh_bx() { int t = blockIdx.x; asm volatile("" : "+s"(t)); return t; }
; __device__ __forceinline__ void conv_gate(const bf16_t* ZB, const bf16_t* ZC, const float* cw, bf16_t* Y, int G) {
;     const int gid = fresh_bx() * NTHR + fresh_tid(), NT = G * NTHR;
;     for (int it = gid; it < T * 256; it += NT) {
;         const int t = it >> 8, col = (it & 255) * 8; const size_t o = (size_t)t * D + col;
;         const u32x4 z0 = *(const u32x4*)(ZC + o), gb = *(const u32x4*)(ZB + o);
;         const u32x4 z1 = (t >= 1) ? *(const u32x4*)(ZC + o - D) : (u32x4){0u, 0u, 0u, 0u}, z2 = (t >= 2) ? *(const u32x4*)(ZC + o - 2 * D) : (u32x4){0u, 0u, 0u, 0u};
;         const f32x4 wa0 = *(const f32x4*)(cw + col), wa1 = *(const f32x4*)(cw + col + 4), wb0 = *(const f32x4*)(cw + D + col), wb1 = *(const f32x4*)(cw + D + col + 4),
;                     wc0 = *(const f32x4*)(cw + 2 * D + col), wc1 = *(const f32x4*)(cw + 2 * D + col + 4);
;         float r[8];
;         r[0] = bf_lo(gb.x) * (wa0[0] * bf_lo(z2.x) + wb0[0] * bf_lo(z1.x) + wc0[0] * bf_lo(z0.x)); r[1] = bf_hi(gb.x) * (wa0[1] * bf_hi(z2.x) + wb0[1] * bf_hi(z1.x) + wc0[1] * bf_hi(z0.x));
;         r[2] = bf_lo(gb.y) * (wa0[2] * bf_lo(z2.y) + wb0[2] * bf_lo(z1.y) + wc0[2] * bf_lo(z0.y)); r[3] = bf_hi(gb.y) * (wa0[3] * bf_hi(z2.y) + wb0[3] * bf_hi(z1.y) + wc0[3] * bf_hi(z0.y));
;         r[4] = bf_lo(gb.z) * (wa1[0] * bf_lo(z2.z) + wb1[0] * bf_lo(z1.z) + wc1[0] * bf_lo(z0.z)); r[5] = bf_hi(gb.z) * (wa1[1] * bf_hi(z2.z) + wb1[1] * bf_hi(z1.z) + wc1[1] * bf_hi(z0.z));
;         r[6] = bf_lo(gb.w) * (wa1[2] * bf_lo(z2.w) + wb1[2] * bf_lo(z1.w) + wc1[2] * bf_lo(z0.w)); r[7] = bf_hi(gb.w) * (wa1[3] * bf_hi(z2.w) + wb1[3] * bf_hi(z1.w) + wc1[3] * bf_hi(z0.w));
;         u32x4 w; w.x = cvt_pk_bf16(r[0], r[1]); w.y = cvt_pk_bf16(r[2], r[3]); w.z = cvt_pk_bf16(r[4], r[5]); w.w = cvt_pk_bf16(r[6], r[7]);
;         *(u32x4*)(Y + o) = w;
;     }
; }
	v_lshlrev_b32_e32 v48, 16, v96
	v_and_b32_e32 v49, s27, v96
	v_lshlrev_b32_e32 v50, 16, v97
	v_and_b32_e32 v51, s27, v97
	v_lshlrev_b32_e32 v52, 16, v98
	v_and_b32_e32 v53, s27, v98
	v_lshlrev_b32_e32 v54, 16, v99
	v_and_b32_e32 v55, s27, v99
	v_lshlrev_b32_e32 v56, 16, v160
	v_and_b32_e32 v57, s27, v160
	v_lshlrev_b32_e32 v58, 16, v161
	v_and_b32_e32 v59, s27, v161
	v_lshlrev_b32_e32 v60, 16, v162
	v_and_b32_e32 v61, s27, v162
	v_lshlrev_b32_e32 v62, 16, v163
	v_and_b32_e32 v63, s27, v163
	v_pk_mul_f32 v[64:65], v[8:9], v[32:33]
	v_pk_mul_f32 v[66:67], v[10:11], v[34:35]
	v_pk_mul_f32 v[68:69], v[12:13], v[36:37]
	v_pk_mul_f32 v[70:71], v[14:15], v[38:39]
	v_pk_fma_f32 v[64:65], v[16:17], v[40:41], v[64:65]
	v_pk_fma_f32 v[66:67], v[18:19], v[42:43], v[66:67]
	v_pk_fma_f32 v[68:69], v[20:21], v[44:45], v[68:69]
	v_pk_fma_f32 v[70:71], v[22:23], v[46:47], v[70:71]
	v_pk_fma_f32 v[64:65], v[24:25], v[48:49], v[64:65]
	v_pk_fma_f32 v[66:67], v[26:27], v[50:51], v[66:67]
	v_pk_fma_f32 v[68:69], v[28:29], v[52:53], v[68:69]
	v_pk_fma_f32 v[70:71], v[30:31], v[54:55], v[70:71]
	v_pk_mul_f32 v[64:65], v[64:65], v[56:57]
	v_pk_mul_f32 v[66:67], v[66:67], v[58:59]
	v_pk_mul_f32 v[68:69], v[68:69], v[60:61]
	v_pk_mul_f32 v[70:71], v[70:71], v[62:63]
	v_cvt_pk_bf16_f32 v72, v64, v65
	v_cvt_pk_bf16_f32 v73, v66, v67
	v_cvt_pk_bf16_f32 v74, v68, v69
	v_cvt_pk_bf16_f32 v75, v70, v71
	global_store_dwordx4 v6, v[72:75], s[14:15]
	s_add_u32 s14, s14, 0x1000
	s_addc_u32 s15, s15, 0
	s_waitcnt vmcnt(26)
	v_lshlrev_b32_e32 v32, 16, v100
	v_and_b32_e32 v33, s27, v100
	v_lshlrev_b32_e32 v34, 16, v101
	v_and_b32_e32 v35, s27, v101
	v_lshlrev_b32_e32 v36, 16, v102
	v_and_b32_e32 v37, s27, v102
	v_lshlrev_b32_e32 v38, 16, v103
	v_and_b32_e32 v39, s27, v103
	v_lshlrev_b32_e32 v56, 16, v164
	v_and_b32_e32 v57, s27, v164
	v_lshlrev_b32_e32 v58, 16, v165
	v_and_b32_e32 v59, s27, v165
	v_lshlrev_b32_e32 v60, 16, v166
	v_and_b32_e32 v61, s27, v166
	v_lshlrev_b32_e32 v62, 16, v167
	v_and_b32_e32 v63, s27, v167
	v_pk_mul_f32 v[64:65], v[8:9], v[40:41]
	v_pk_mul_f32 v[66:67], v[10:11], v[42:43]
	v_pk_mul_f32 v[68:69], v[12:13], v[44:45]
	v_pk_mul_f32 v[70:71], v[14:15], v[46:47]
	v_pk_fma_f32 v[64:65], v[16:17], v[48:49], v[64:65]
	v_pk_fma_f32 v[66:67], v[18:19], v[50:51], v[66:67]
	v_pk_fma_f32 v[68:69], v[20:21], v[52:53], v[68:69]
	v_pk_fma_f32 v[70:71], v[22:23], v[54:55], v[70:71]
	v_pk_fma_f32 v[64:65], v[24:25], v[32:33], v[64:65]
	v_pk_fma_f32 v[66:67], v[26:27], v[34:35], v[66:67]
	v_pk_fma_f32 v[68:69], v[28:29], v[36:37], v[68:69]
	v_pk_fma_f32 v[70:71], v[30:31], v[38:39], v[70:71]
	v_pk_mul_f32 v[64:65], v[64:65], v[56:57]
	v_pk_mul_f32 v[66:67], v[66:67], v[58:59]
	v_pk_mul_f32 v[68:69], v[68:69], v[60:61]
	v_pk_mul_f32 v[70:71], v[70:71], v[62:63]
	v_cvt_pk_bf16_f32 v72, v64, v65
	v_cvt_pk_bf16_f32 v73, v66, v67
	v_cvt_pk_bf16_f32 v74, v68, v69
	v_cvt_pk_bf16_f32 v75, v70, v71
	global_store_dwordx4 v6, v[72:75], s[14:15]
	s_add_u32 s14, s14, 0x1000
	s_addc_u32 s15, s15, 0
	s_waitcnt vmcnt(25)
	v_lshlrev_b32_e32 v40, 16, v104
	v_and_b32_e32 v41, s27, v104
	v_lshlrev_b32_e32 v42, 16, v105
	v_and_b32_e32 v43, s27, v105
	v_lshlrev_b32_e32 v44, 16, v106
	v_and_b32_e32 v45, s27, v106
	v_lshlrev_b32_e32 v46, 16, v107
	v_and_b32_e32 v47, s27, v107
	v_lshlrev_b32_e32 v56, 16, v168
	v_and_b32_e32 v57, s27, v168
	v_lshlrev_b32_e32 v58, 16, v169
	v_and_b32_e32 v59, s27, v169
	v_lshlrev_b32_e32 v60, 16, v170
	v_and_b32_e32 v61, s27, v170
	v_lshlrev_b32_e32 v62, 16, v171
	v_and_b32_e32 v63, s27, v171
	v_pk_mul_f32 v[64:65], v[8:9], v[48:49]
	v_pk_mul_f32 v[66:67], v[10:11], v[50:51]
	v_pk_mul_f32 v[68:69], v[12:13], v[52:53]
	v_pk_mul_f32 v[70:71], v[14:15], v[54:55]
	v_pk_fma_f32 v[64:65], v[16:17], v[32:33], v[64:65]
	v_pk_fma_f32 v[66:67], v[18:19], v[34:35], v[66:67]
	v_pk_fma_f32 v[68:69], v[20:21], v[36:37], v[68:69]
	v_pk_fma_f32 v[70:71], v[22:23], v[38:39], v[70:71]
	v_pk_fma_f32 v[64:65], v[24:25], v[40:41], v[64:65]
	v_pk_fma_f32 v[66:67], v[26:27], v[42:43], v[66:67]
	v_pk_fma_f32 v[68:69], v[28:29], v[44:45], v[68:69]
	v_pk_fma_f32 v[70:71], v[30:31], v[46:47], v[70:71]
	v_pk_mul_f32 v[64:65], v[64:65], v[56:57]
	v_pk_mul_f32 v[66:67], v[66:67], v[58:59]
	v_pk_mul_f32 v[68:69], v[68:69], v[60:61]
	v_pk_mul_f32 v[70:71], v[70:71], v[62:63]
	v_cvt_pk_bf16_f32 v72, v64, v65
	v_cvt_pk_bf16_f32 v73, v66, v67
	v_cvt_pk_bf16_f32 v74, v68, v69
	v_cvt_pk_bf16_f32 v75, v70, v71
	global_store_dwordx4 v6, v[72:75], s[14:15]
	s_add_u32 s14, s14, 0x1000
	s_addc_u32 s15, s15, 0
	s_waitcnt vmcnt(24)
	v_lshlrev_b32_e32 v48, 16, v108
	v_and_b32_e32 v49, s27, v108
	v_lshlrev_b32_e32 v50, 16, v109
	v_and_b32_e32 v51, s27, v109
	v_lshlrev_b32_e32 v52, 16, v110
	v_and_b32_e32 v53, s27, v110
	v_lshlrev_b32_e32 v54, 16, v111
	v_and_b32_e32 v55, s27, v111
	v_lshlrev_b32_e32 v56, 16, v172
	v_and_b32_e32 v57, s27, v172
	v_lshlrev_b32_e32 v58, 16, v173
	v_and_b32_e32 v59, s27, v173
	v_lshlrev_b32_e32 v60, 16, v174
	v_and_b32_e32 v61, s27, v174
	v_lshlrev_b32_e32 v62, 16, v175
	v_and_b32_e32 v63, s27, v175
	v_pk_mul_f32 v[64:65], v[8:9], v[32:33]
	v_pk_mul_f32 v[66:67], v[10:11], v[34:35]
	v_pk_mul_f32 v[68:69], v[12:13], v[36:37]
	v_pk_mul_f32 v[70:71], v[14:15], v[38:39]
	v_pk_fma_f32 v[64:65], v[16:17], v[40:41], v[64:65]
	v_pk_fma_f32 v[66:67], v[18:19], v[42:43], v[66:67]
	v_pk_fma_f32 v[68:69], v[20:21], v[44:45], v[68:69]
	v_pk_fma_f32 v[70:71], v[22:23], v[46:47], v[70:71]
	v_pk_fma_f32 v[64:65], v[24:25], v[48:49], v[64:65]
	v_pk_fma_f32 v[66:67], v[26:27], v[50:51], v[66:67]
	v_pk_fma_f32 v[68:69], v[28:29], v[52:53], v[68:69]
	v_pk_fma_f32 v[70:71], v[30:31], v[54:55], v[70:71]
	v_pk_mul_f32 v[64:65], v[64:65], v[56:57]
	v_pk_mul_f32 v[66:67], v[66:67], v[58:59]
	v_pk_mul_f32 v[68:69], v[68:69], v[60:61]
	v_pk_mul_f32 v[70:71], v[70:71], v[62:63]
	v_cvt_pk_bf16_f32 v72, v64, v65
	v_cvt_pk_bf16_f32 v73, v66, v67
	v_cvt_pk_bf16_f32 v74, v68, v69
	v_cvt_pk_bf16_f32 v75, v70, v71
	global_store_dwordx4 v6, v[72:75], s[14:15]
	s_add_u32 s14, s14, 0x1000
	s_addc_u32 s15, s15, 0
	s_waitcnt vmcnt(23)
; __device__ __forceinline__ unsigned cvt_pk_bf16(float lo, float hi) { unsigned r; asm volatile("v_cvt_pk_bf16_f32 %0, %1, %2" : "=v"(r) : "v"(lo), "v"(hi)); return r; }
; __device__ __forceinline__ int fresh_tid() { int t = threadIdx.x; asm volatile("" : "+v"(t)); return t; }
; __device__ __forceinline__ int fresh_bx() { int t = blockIdx.x; asm volatile("" : "+s"(t)); return t; }
; __device__ __forceinline__ void conv_gate(const bf16_t* ZB, const bf16_t* ZC, const float* cw, bf16_t* Y, int G) {
;     const int gid = fresh_bx() * NTHR + fresh_tid(), NT = G * NTHR;
;     for (int it = gid; it < T * 256; it += NT) {
;         const int t = it >> 8, col = (it & 255) * 8; const size_t o = (size_t)t * D + col;
;         const u32x4 z0 = *(const u32x4*)(ZC + o), gb = *(const u32x4*)(ZB + o);
;         const u32x4 z1 = (t >= 1) ? *(const u32x4*)(ZC + o - D) : (u32x4){0u, 0u, 0u, 0u}, z2 = (t >= 2) ? *(const u32x4*)(ZC + o - 2 * D) : (u32x4){0u, 0u, 0u, 0u};
;         const f32x4 wa0 = *(const f32x4*)(cw + col), wa1 = *(const f32x4*)(cw + col + 4), wb0 = *(const f32x4*)(cw + D + col), wb1 = *(const f32x4*)(cw + D + col + 4),
;                     wc0 = *(const f32x4*)(cw + 2 * D + col), wc1 = *(const f32x4*)(cw + 2 * D + col + 4);
;         float r[8];
;         r[0] = bf_lo(gb.x) * (wa0[0] * bf_lo(z2.x) + wb0[0] * bf_lo(z1.x) + wc0[0] * bf_lo(z0.x)); r[1] = bf_hi(gb.x) * (wa0[1] * bf_hi(z2.x) + wb0[1] * bf_hi(z1.x) + wc0[1] * bf_hi(z0.x));
;         r[2] = bf_lo(gb.y) * (wa0[2] * bf_lo(z2.y) + wb0[2] * bf_lo(z1.y) + wc0[2] * bf_lo(z0.y)); r[3] = bf_hi(gb.y) * (wa0[3] * bf_hi(z2.y) + wb0[3] * bf_hi(z1.y) + wc0[3] * bf_hi(z0.y));
;         r[4] = bf_lo(gb.z) * (wa1[0] * bf_lo(z2.z) + wb1[0] * bf_lo(z1.z) + wc1[0] * bf_lo(z0.z)); r[5] = bf_hi(gb.z) * (wa1[1] * bf_hi(z2.z) + wb1[1] * bf_hi(z1.z) + wc1[1] * bf_hi(z0.z));
;         r[6] = bf_lo(gb.w) * (wa1[2] * bf_lo(z2.w) + wb1[2] * bf_lo(z1.w) + wc1[2] * bf_lo(z0.w)); r[7] = bf_hi(gb.w) * (wa1[3] * bf_hi(z2.w) + wb1[3] * bf_hi(z1.w) + wc1[3] * bf_hi(z0.w));
;         u32x4 w; w.x = cvt_pk_bf16(r[0], r[1]); w.y = cvt_pk_bf16(r[2], r[3]); w.z = cvt_pk_bf16(r[4], r[5]); w.w = cvt_pk_bf16(r[6], r[7]);
;         *(u32x4*)(Y + o) = w;
;     }
; }
	v_lshlrev_b32_e32 v32, 16, v112
	v_and_b32_e32 v33, s27, v112
	v_lshlrev_b32_e32 v34, 16, v113
	v_and_b32_e32 v35, s27, v113
	v_lshlrev_b32_e32 v36, 16, v114
	v_and_b32_e32 v37, s27, v114
	v_lshlrev_b32_e32 v38, 16, v115
	v_and_b32_e32 v39, s27, v115
	v_lshlrev_b32_e32 v56, 16, v176
	v_and_b32_e32 v57, s27, v176
	v_lshlrev_b32_e32 v58, 16, v177
	v_and_b32_e32 v59, s27, v177
	v_lshlrev_b32_e32 v60, 16, v178
	v_and_b32_e32 v61, s27, v178
	v_lshlrev_b32_e32 v62, 16, v179
	v_and_b32_e32 v63, s27, v179
	v_pk_mul_f32 v[64:65], v[8:9], v[40:41]
	v_pk_mul_f32 v[66:67], v[10:11], v[42:43]
	v_pk_mul_f32 v[68:69], v[12:13], v[44:45]
	v_pk_mul_f32 v[70:71], v[14:15], v[46:47]
	v_pk_fma_f32 v[64:65], v[16:17], v[48:49], v[64:65]
	v_pk_fma_f32 v[66:67], v[18:19], v[50:51], v[66:67]
	v_pk_fma_f32 v[68:69], v[20:21], v[52:53], v[68:69]
	v_pk_fma_f32 v[70:71], v[22:23], v[54:55], v[70:71]
	v_pk_fma_f32 v[64:65], v[24:25], v[32:33], v[64:65]
	v_pk_fma_f32 v[66:67], v[26:27], v[34:35], v[66:67]
	v_pk_fma_f32 v[68:69], v[28:29], v[36:37], v[68:69]
	v_pk_fma_f32 v[70:71], v[30:31], v[38:39], v[70:71]
	v_pk_mul_f32 v[64:65], v[64:65], v[56:57]
	v_pk_mul_f32 v[66:67], v[66:67], v[58:59]
	v_pk_mul_f32 v[68:69], v[68:69], v[60:61]
	v_pk_mul_f32 v[70:71], v[70:71], v[62:63]
	v_cvt_pk_bf16_f32 v72, v64, v65
	v_cvt_pk_bf16_f32 v73, v66, v67
	v_cvt_pk_bf16_f32 v74, v68, v69
	v_cvt_pk_bf16_f32 v75, v70, v71
	global_store_dwordx4 v6, v[72:75], s[14:15]
	s_add_u32 s14, s14, 0x1000
	s_addc_u32 s15, s15, 0
	s_waitcnt vmcnt(22)
	v_lshlrev_b32_e32 v40, 16, v116
	v_and_b32_e32 v41, s27, v116
	v_lshlrev_b32_e32 v42, 16, v117
	v_and_b32_e32 v43, s27, v117
	v_lshlrev_b32_e32 v44, 16, v118
	v_and_b32_e32 v45, s27, v118
	v_lshlrev_b32_e32 v46, 16, v119
	v_and_b32_e32 v47, s27, v119
	v_lshlrev_b32_e32 v56, 16, v180
	v_and_b32_e32 v57, s27, v180
	v_lshlrev_b32_e32 v58, 16, v181
	v_and_b32_e32 v59, s27, v181
	v_lshlrev_b32_e32 v60, 16, v182
	v_and_b32_e32 v61, s27, v182
	v_lshlrev_b32_e32 v62, 16, v183
	v_and_b32_e32 v63, s27, v183
	v_pk_mul_f32 v[64:65], v[8:9], v[48:49]
	v_pk_mul_f32 v[66:67], v[10:11], v[50:51]
	v_pk_mul_f32 v[68:69], v[12:13], v[52:53]
	v_pk_mul_f32 v[70:71], v[14:15], v[54:55]
	v_pk_fma_f32 v[64:65], v[16:17], v[32:33], v[64:65]
	v_pk_fma_f32 v[66:67], v[18:19], v[34:35], v[66:67]
	v_pk_fma_f32 v[68:69], v[20:21], v[36:37], v[68:69]
	v_pk_fma_f32 v[70:71], v[22:23], v[38:39], v[70:71]
	v_pk_fma_f32 v[64:65], v[24:25], v[40:41], v[64:65]
	v_pk_fma_f32 v[66:67], v[26:27], v[42:43], v[66:67]
	v_pk_fma_f32 v[68:69], v[28:29], v[44:45], v[68:69]
	v_pk_fma_f32 v[70:71], v[30:31], v[46:47], v[70:71]
	v_pk_mul_f32 v[64:65], v[64:65], v[56:57]
	v_pk_mul_f32 v[66:67], v[66:67], v[58:59]
	v_pk_mul_f32 v[68:69], v[68:69], v[60:61]
	v_pk_mul_f32 v[70:71], v[70:71], v[62:63]
	v_cvt_pk_bf16_f32 v72, v64, v65
	v_cvt_pk_bf16_f32 v73, v66, v67
	v_cvt_pk_bf16_f32 v74, v68, v69
	v_cvt_pk_bf16_f32 v75, v70, v71
	global_store_dwordx4 v6, v[72:75], s[14:15]
	s_add_u32 s14, s14, 0x1000
	s_addc_u32 s15, s15, 0
	s_waitcnt vmcnt(21)
	v_lshlrev_b32_e32 v48, 16, v120
	v_and_b32_e32 v49, s27, v120
	v_lshlrev_b32_e32 v50, 16, v121
	v_and_b32_e32 v51, s27, v121
	v_lshlrev_b32_e32 v52, 16, v122
	v_and_b32_e32 v53, s27, v122
	v_lshlrev_b32_e32 v54, 16, v123
	v_and_b32_e32 v55, s27, v123
	v_lshlrev_b32_e32 v56, 16, v184
	v_and_b32_e32 v57, s27, v184
	v_lshlrev_b32_e32 v58, 16, v185
	v_and_b32_e32 v59, s27, v185
	v_lshlrev_b32_e32 v60, 16, v186
	v_and_b32_e32 v61, s27, v186
	v_lshlrev_b32_e32 v62, 16, v187
	v_and_b32_e32 v63, s27, v187
	v_pk_mul_f32 v[64:65], v[8:9], v[32:33]
	v_pk_mul_f32 v[66:67], v[10:11], v[34:35]
	v_pk_mul_f32 v[68:69], v[12:13], v[36:37]
	v_pk_mul_f32 v[70:71], v[14:15], v[38:39]
	v_pk_fma_f32 v[64:65], v[16:17], v[40:41], v[64:65]
	v_pk_fma_f32 v[66:67], v[18:19], v[42:43], v[66:67]
	v_pk_fma_f32 v[68:69], v[20:21], v[44:45], v[68:69]
	v_pk_fma_f32 v[70:71], v[22:23], v[46:47], v[70:71]
	v_pk_fma_f32 v[64:65], v[24:25], v[48:49], v[64:65]
	v_pk_fma_f32 v[66:67], v[26:27], v[50:51], v[66:67]
	v_pk_fma_f32 v[68:69], v[28:29], v[52:53], v[68:69]
	v_pk_fma_f32 v[70:71], v[30:31], v[54:55], v[70:71]
	v_pk_mul_f32 v[64:65], v[64:65], v[56:57]
	v_pk_mul_f32 v[66:67], v[66:67], v[58:59]
	v_pk_mul_f32 v[68:69], v[68:69], v[60:61]
	v_pk_mul_f32 v[70:71], v[70:71], v[62:63]
	v_cvt_pk_bf16_f32 v72, v64, v65
	v_cvt_pk_bf16_f32 v73, v66, v67
	v_cvt_pk_bf16_f32 v74, v68, v69
	v_cvt_pk_bf16_f32 v75, v70, v71
	global_store_dwordx4 v6, v[72:75], s[14:15]
	s_add_u32 s14, s14, 0x1000
	s_addc_u32 s15, s15, 0
	s_waitcnt vmcnt(20)
	v_lshlrev_b32_e32 v32, 16, v124
	v_and_b32_e32 v33, s27, v124
	v_lshlrev_b32_e32 v34, 16, v125
	v_and_b32_e32 v35, s27, v125
	v_lshlrev_b32_e32 v36, 16, v126
	v_and_b32_e32 v37, s27, v126
	v_lshlrev_b32_e32 v38, 16, v127
	v_and_b32_e32 v39, s27, v127
	v_lshlrev_b32_e32 v56, 16, v188
	v_and_b32_e32 v57, s27, v188
	v_lshlrev_b32_e32 v58, 16, v189
	v_and_b32_e32 v59, s27, v189
	v_lshlrev_b32_e32 v60, 16, v190
	v_and_b32_e32 v61, s27, v190
	v_lshlrev_b32_e32 v62, 16, v191
	v_and_b32_e32 v63, s27, v191
	v_pk_mul_f32 v[64:65], v[8:9], v[40:41]
	v_pk_mul_f32 v[66:67], v[10:11], v[42:43]
	v_pk_mul_f32 v[68:69], v[12:13], v[44:45]
	v_pk_mul_f32 v[70:71], v[14:15], v[46:47]
	v_pk_fma_f32 v[64:65], v[16:17], v[48:49], v[64:65]
	v_pk_fma_f32 v[66:67], v[18:19], v[50:51], v[66:67]
	v_pk_fma_f32 v[68:69], v[20:21], v[52:53], v[68:69]
	v_pk_fma_f32 v[70:71], v[22:23], v[54:55], v[70:71]
	v_pk_fma_f32 v[64:65], v[24:25], v[32:33], v[64:65]
	v_pk_fma_f32 v[66:67], v[26:27], v[34:35], v[66:67]
	v_pk_fma_f32 v[68:69], v[28:29], v[36:37], v[68:69]
	v_pk_fma_f32 v[70:71], v[30:31], v[38:39], v[70:71]
	v_pk_mul_f32 v[64:65], v[64:65], v[56:57]
	v_pk_mul_f32 v[66:67], v[66:67], v[58:59]
	v_pk_mul_f32 v[68:69], v[68:69], v[60:61]
	v_pk_mul_f32 v[70:71], v[70:71], v[62:63]
	v_cvt_pk_bf16_f32 v72, v64, v65
	v_cvt_pk_bf16_f32 v73, v66, v67
	v_cvt_pk_bf16_f32 v74, v68, v69
	v_cvt_pk_bf16_f32 v75, v70, v71
	global_store_dwordx4 v6, v[72:75], s[14:15]
	s_add_u32 s14, s14, 0x1000
	s_addc_u32 s15, s15, 0
	s_waitcnt vmcnt(19)
; __device__ __forceinline__ unsigned cvt_pk_bf16(float lo, float hi) { unsigned r; asm volatile("v_cvt_pk_bf16_f32 %0, %1, %2" : "=v"(r) : "v"(lo), "v"(hi)); return r; }
; __device__ __forceinline__ int fresh_tid() { int t = threadIdx.x; asm volatile("" : "+v"(t)); return t; }
; __device__ __forceinline__ int fresh_bx() { int t = blockIdx.x; asm volatile("" : "+s"(t)); return t; }
; __device__ __forceinline__ void conv_gate(const bf16_t* ZB, const bf16_t* ZC, const float* cw, bf16_t* Y, int G) {
;     const int gid = fresh_bx() * NTHR + fresh_tid(), NT = G * NTHR;
;     for (int it = gid; it < T * 256; it += NT) {
;         const int t = it >> 8, col = (it & 255) * 8; const size_t o = (size_t)t * D + col;
;         const u32x4 z0 = *(const u32x4*)(ZC + o), gb = *(const u32x4*)(ZB + o);
;         const u32x4 z1 = (t >= 1) ? *(const u32x4*)(ZC + o - D) : (u32x4){0u, 0u, 0u, 0u}, z2 = (t >= 2) ? *(const u32x4*)(ZC + o - 2 * D) : (u32x4){0u, 0u, 0u, 0u};
;         const f32x4 wa0 = *(const f32x4*)(cw + col), wa1 = *(const f32x4*)(cw + col + 4), wb0 = *(const f32x4*)(cw + D + col), wb1 = *(const f32x4*)(cw + D + col + 4),
;                     wc0 = *(const f32x4*)(cw + 2 * D + col), wc1 = *(const f32x4*)(cw + 2 * D + col + 4);
;         float r[8];
;         r[0] = bf_lo(gb.x) * (wa0[0] * bf_lo(z2.x) + wb0[0] * bf_lo(z1.x) + wc0[0] * bf_lo(z0.x)); r[1] = bf_hi(gb.x) * (wa0[1] * bf_hi(z2.x) + wb0[1] * bf_hi(z1.x) + wc0[1] * bf_hi(z0.x));
;         r[2] = bf_lo(gb.y) * (wa0[2] * bf_lo(z2.y) + wb0[2] * bf_lo(z1.y) + wc0[2] * bf_lo(z0.y)); r[3] = bf_hi(gb.y) * (wa0[3] * bf_hi(z2.y) + wb0[3] * bf_hi(z1.y) + wc0[3] * bf_hi(z0.y));
;         r[4] = bf_lo(gb.z) * (wa1[0] * bf_lo(z2.z) + wb1[0] * bf_lo(z1.z) + wc1[0] * bf_lo(z0.z)); r[5] = bf_hi(gb.z) * (wa1[1] * bf_hi(z2.z) + wb1[1] * bf_hi(z1.z) + wc1[1] * bf_hi(z0.z));
;         r[6] = bf_lo(gb.w) * (wa1[2] * bf_lo(z2.w) + wb1[2] * bf_lo(z1.w) + wc1[2] * bf_lo(z0.w)); r[7] = bf_hi(gb.w) * (wa1[3] * bf_hi(z2.w) + wb1[3] * bf_hi(z1.w) + wc1[3] * bf_hi(z0.w));
;         u32x4 w; w.x = cvt_pk_bf16(r[0], r[1]); w.y = cvt_pk_bf16(r[2], r[3]); w.z = cvt_pk_bf16(r[4], r[5]); w.w = cvt_pk_bf16(r[6], r[7]);
;         *(u32x4*)(Y + o) = w;
;     }
; }
	v_lshlrev_b32_e32 v40, 16, v128
	v_and_b32_e32 v41, s27, v128
	v_lshlrev_b32_e32 v42, 16, v129
	v_and_b32_e32 v43, s27, v129
	v_lshlrev_b32_e32 v44, 16, v130
	v_and_b32_e32 v45, s27, v130
	v_lshlrev_b32_e32 v46, 16, v131
	v_and_b32_e32 v47, s27, v131
	v_lshlrev_b32_e32 v56, 16, v192
	v_and_b32_e32 v57, s27, v192
	v_lshlrev_b32_e32 v58, 16, v193
	v_and_b32_e32 v59, s27, v193
	v_lshlrev_b32_e32 v60, 16, v194
	v_and_b32_e32 v61, s27, v194
	v_lshlrev_b32_e32 v62, 16, v195
	v_and_b32_e32 v63, s27, v195
	v_pk_mul_f32 v[64:65], v[8:9], v[48:49]
	v_pk_mul_f32 v[66:67], v[10:11], v[50:51]
	v_pk_mul_f32 v[68:69], v[12:13], v[52:53]
	v_pk_mul_f32 v[70:71], v[14:15], v[54:55]
	v_pk_fma_f32 v[64:65], v[16:17], v[32:33], v[64:65]
	v_pk_fma_f32 v[66:67], v[18:19], v[34:35], v[66:67]
	v_pk_fma_f32 v[68:69], v[20:21], v[36:37], v[68:69]
	v_pk_fma_f32 v[70:71], v[22:23], v[38:39], v[70:71]
	v_pk_fma_f32 v[64:65], v[24:25], v[40:41], v[64:65]
	v_pk_fma_f32 v[66:67], v[26:27], v[42:43], v[66:67]
	v_pk_fma_f32 v[68:69], v[28:29], v[44:45], v[68:69]
	v_pk_fma_f32 v[70:71], v[30:31], v[46:47], v[70:71]
	v_pk_mul_f32 v[64:65], v[64:65], v[56:57]
	v_pk_mul_f32 v[66:67], v[66:67], v[58:59]
	v_pk_mul_f32 v[68:69], v[68:69], v[60:61]
	v_pk_mul_f32 v[70:71], v[70:71], v[62:63]
	v_cvt_pk_bf16_f32 v72, v64, v65
	v_cvt_pk_bf16_f32 v73, v66, v67
	v_cvt_pk_bf16_f32 v74, v68, v69
	v_cvt_pk_bf16_f32 v75, v70, v71
	global_store_dwordx4 v6, v[72:75], s[14:15]
	s_add_u32 s14, s14, 0x1000
	s_addc_u32 s15, s15, 0
	s_waitcnt vmcnt(18)
	v_lshlrev_b32_e32 v48, 16, v132
	v_and_b32_e32 v49, s27, v132
	v_lshlrev_b32_e32 v50, 16, v133
	v_and_b32_e32 v51, s27, v133
	v_lshlrev_b32_e32 v52, 16, v134
	v_and_b32_e32 v53, s27, v134
	v_lshlrev_b32_e32 v54, 16, v135
	v_and_b32_e32 v55, s27, v135
	v_lshlrev_b32_e32 v56, 16, v196
	v_and_b32_e32 v57, s27, v196
	v_lshlrev_b32_e32 v58, 16, v197
	v_and_b32_e32 v59, s27, v197
	v_lshlrev_b32_e32 v60, 16, v198
	v_and_b32_e32 v61, s27, v198
	v_lshlrev_b32_e32 v62, 16, v199
	v_and_b32_e32 v63, s27, v199
	v_pk_mul_f32 v[64:65], v[8:9], v[32:33]
	v_pk_mul_f32 v[66:67], v[10:11], v[34:35]
	v_pk_mul_f32 v[68:69], v[12:13], v[36:37]
	v_pk_mul_f32 v[70:71], v[14:15], v[38:39]
	v_pk_fma_f32 v[64:65], v[16:17], v[40:41], v[64:65]
	v_pk_fma_f32 v[66:67], v[18:19], v[42:43], v[66:67]
	v_pk_fma_f32 v[68:69], v[20:21], v[44:45], v[68:69]
	v_pk_fma_f32 v[70:71], v[22:23], v[46:47], v[70:71]
	v_pk_fma_f32 v[64:65], v[24:25], v[48:49], v[64:65]
	v_pk_fma_f32 v[66:67], v[26:27], v[50:51], v[66:67]
	v_pk_fma_f32 v[68:69], v[28:29], v[52:53], v[68:69]
	v_pk_fma_f32 v[70:71], v[30:31], v[54:55], v[70:71]
	v_pk_mul_f32 v[64:65], v[64:65], v[56:57]
	v_pk_mul_f32 v[66:67], v[66:67], v[58:59]
	v_pk_mul_f32 v[68:69], v[68:69], v[60:61]
	v_pk_mul_f32 v[70:71], v[70:71], v[62:63]
	v_cvt_pk_bf16_f32 v72, v64, v65
	v_cvt_pk_bf16_f32 v73, v66, v67
	v_cvt_pk_bf16_f32 v74, v68, v69
	v_cvt_pk_bf16_f32 v75, v70, v71
	global_store_dwordx4 v6, v[72:75], s[14:15]
	s_add_u32 s14, s14, 0x1000
	s_addc_u32 s15, s15, 0
	s_waitcnt vmcnt(17)
; __device__ __forceinline__ unsigned cvt_pk_bf16(float lo, float hi) { unsigned r; asm volatile("v_cvt_pk_bf16_f32 %0, %1, %2" : "=v"(r) : "v"(lo), "v"(hi)); return r; }
; __device__ __forceinline__ int fresh_tid() { int t = threadIdx.x; asm volatile("" : "+v"(t)); return t; }
; __device__ __forceinline__ int fresh_bx() { int t = blockIdx.x; asm volatile("" : "+s"(t)); return t; }
; __device__ __forceinline__ void conv_gate(const bf16_t* ZB, const bf16_t* ZC, const float* cw, bf16_t* Y, int G) {
;     const int gid = fresh_bx() * NTHR + fresh_tid(), NT = G * NTHR;
;     for (int it = gid; it < T * 256; it += NT) {
;         const int t = it >> 8, col = (it & 255) * 8; const size_t o = (size_t)t * D + col;
;         const u32x4 z0 = *(const u32x4*)(ZC + o), gb = *(const u32x4*)(ZB + o);
;         const u32x4 z1 = (t >= 1) ? *(const u32x4*)(ZC + o - D) : (u32x4){0u, 0u, 0u, 0u}, z2 = (t >= 2) ? *(const u32x4*)(ZC + o - 2 * D) : (u32x4){0u, 0u, 0u, 0u};
;         const f32x4 wa0 = *(const f32x4*)(cw + col), wa1 = *(const f32x4*)(cw + col + 4), wb0 = *(const f32x4*)(cw + D + col), wb1 = *(const f32x4*)(cw + D + col + 4),
;                     wc0 = *(const f32x4*)(cw + 2 * D + col), wc1 = *(const f32x4*)(cw + 2 * D + col + 4);
;         float r[8];
;         r[0] = bf_lo(gb.x) * (wa0[0] * bf_lo(z2.x) + wb0[0] * bf_lo(z1.x) + wc0[0] * bf_lo(z0.x)); r[1] = bf_hi(gb.x) * (wa0[1] * bf_hi(z2.x) + wb0[1] * bf_hi(z1.x) + wc0[1] * bf_hi(z0.x));
;         r[2] = bf_lo(gb.y) * (wa0[2] * bf_lo(z2.y) + wb0[2] * bf_lo(z1.y) + wc0[2] * bf_lo(z0.y)); r[3] = bf_hi(gb.y) * (wa0[3] * bf_hi(z2.y) + wb0[3] * bf_hi(z1.y) + wc0[3] * bf_hi(z0.y));
;         r[4] = bf_lo(gb.z) * (wa1[0] * bf_lo(z2.z) + wb1[0] * bf_lo(z1.z) + wc1[0] * bf_lo(z0.z)); r[5] = bf_hi(gb.z) * (wa1[1] * bf_hi(z2.z) + wb1[1] * bf_hi(z1.z) + wc1[1] * bf_hi(z0.z));
;         r[6] = bf_lo(gb.w) * (wa1[2] * bf_lo(z2.w) + wb1[2] * bf_lo(z1.w) + wc1[2] * bf_lo(z0.w)); r[7] = bf_hi(gb.w) * (wa1[3] * bf_hi(z2.w) + wb1[3] * bf_hi(z1.w) + wc1[3] * bf_hi(z0.w));
;         u32x4 w; w.x = cvt_pk_bf16(r[0], r[1]); w.y = cvt_pk_bf16(r[2], r[3]); w.z = cvt_pk_bf16(r[4], r[5]); w.w = cvt_pk_bf16(r[6], r[7]);
;         *(u32x4*)(Y + o) = w;
;     }
; }
	v_lshlrev_b32_e32 v32, 16, v136
	v_and_b32_e32 v33, s27, v136
	v_lshlrev_b32_e32 v34, 16, v137
	v_and_b32_e32 v35, s27, v137
	v_lshlrev_b32_e32 v36, 16, v138
	v_and_b32_e32 v37, s27, v138
	v_lshlrev_b32_e32 v38, 16, v139
	v_and_b32_e32 v39, s27, v139
	v_lshlrev_b32_e32 v56, 16, v200
	v_and_b32_e32 v57, s27, v200
	v_lshlrev_b32_e32 v58, 16, v201
	v_and_b32_e32 v59, s27, v201
	v_lshlrev_b32_e32 v60, 16, v202
	v_and_b32_e32 v61, s27, v202
	v_lshlrev_b32_e32 v62, 16, v203
	v_and_b32_e32 v63, s27, v203
	v_pk_mul_f32 v[64:65], v[8:9], v[40:41]
	v_pk_mul_f32 v[66:67], v[10:11], v[42:43]
	v_pk_mul_f32 v[68:69], v[12:13], v[44:45]
	v_pk_mul_f32 v[70:71], v[14:15], v[46:47]
	v_pk_fma_f32 v[64:65], v[16:17], v[48:49], v[64:65]
	v_pk_fma_f32 v[66:67], v[18:19], v[50:51], v[66:67]
	v_pk_fma_f32 v[68:69], v[20:21], v[52:53], v[68:69]
	v_pk_fma_f32 v[70:71], v[22:23], v[54:55], v[70:71]
	v_pk_fma_f32 v[64:65], v[24:25], v[32:33], v[64:65]
	v_pk_fma_f32 v[66:67], v[26:27], v[34:35], v[66:67]
	v_pk_fma_f32 v[68:69], v[28:29], v[36:37], v[68:69]
	v_pk_fma_f32 v[70:71], v[30:31], v[38:39], v[70:71]
	v_pk_mul_f32 v[64:65], v[64:65], v[56:57]
	v_pk_mul_f32 v[66:67], v[66:67], v[58:59]
	v_pk_mul_f32 v[68:69], v[68:69], v[60:61]
	v_pk_mul_f32 v[70:71], v[70:71], v[62:63]
	v_cvt_pk_bf16_f32 v72, v64, v65
	v_cvt_pk_bf16_f32 v73, v66, v67
	v_cvt_pk_bf16_f32 v74, v68, v69
	v_cvt_pk_bf16_f32 v75, v70, v71
	global_store_dwordx4 v6, v[72:75], s[14:15]
	s_add_u32 s14, s14, 0x1000
	s_addc_u32 s15, s15, 0
	s_waitcnt vmcnt(16)
	v_lshlrev_b32_e32 v40, 16, v140
	v_and_b32_e32 v41, s27, v140
	v_lshlrev_b32_e32 v42, 16, v141
	v_and_b32_e32 v43, s27, v141
	v_lshlrev_b32_e32 v44, 16, v142
	v_and_b32_e32 v45, s27, v142
	v_lshlrev_b32_e32 v46, 16, v143
	v_and_b32_e32 v47, s27, v143
	v_lshlrev_b32_e32 v56, 16, v204
	v_and_b32_e32 v57, s27, v204
	v_lshlrev_b32_e32 v58, 16, v205
	v_and_b32_e32 v59, s27, v205
	v_lshlrev_b32_e32 v60, 16, v206
	v_and_b32_e32 v61, s27, v206
	v_lshlrev_b32_e32 v62, 16, v207
	v_and_b32_e32 v63, s27, v207
	v_pk_mul_f32 v[64:65], v[8:9], v[48:49]
	v_pk_mul_f32 v[66:67], v[10:11], v[50:51]
	v_pk_mul_f32 v[68:69], v[12:13], v[52:53]
	v_pk_mul_f32 v[70:71], v[14:15], v[54:55]
	v_pk_fma_f32 v[64:65], v[16:17], v[32:33], v[64:65]
	v_pk_fma_f32 v[66:67], v[18:19], v[34:35], v[66:67]
	v_pk_fma_f32 v[68:69], v[20:21], v[36:37], v[68:69]
	v_pk_fma_f32 v[70:71], v[22:23], v[38:39], v[70:71]
	v_pk_fma_f32 v[64:65], v[24:25], v[40:41], v[64:65]
	v_pk_fma_f32 v[66:67], v[26:27], v[42:43], v[66:67]
	v_pk_fma_f32 v[68:69], v[28:29], v[44:45], v[68:69]
	v_pk_fma_f32 v[70:71], v[30:31], v[46:47], v[70:71]
	v_pk_mul_f32 v[64:65], v[64:65], v[56:57]
	v_pk_mul_f32 v[66:67], v[66:67], v[58:59]
	v_pk_mul_f32 v[68:69], v[68:69], v[60:61]
	v_pk_mul_f32 v[70:71], v[70:71], v[62:63]
	v_cvt_pk_bf16_f32 v72, v64, v65
	v_cvt_pk_bf16_f32 v73, v66, v67
	v_cvt_pk_bf16_f32 v74, v68, v69
	v_cvt_pk_bf16_f32 v75, v70, v71
	global_store_dwordx4 v6, v[72:75], s[14:15]
	s_add_u32 s14, s14, 0x1000
	s_addc_u32 s15, s15, 0
	s_waitcnt vmcnt(15)
	v_lshlrev_b32_e32 v48, 16, v144
	v_and_b32_e32 v49, s27, v144
	v_lshlrev_b32_e32 v50, 16, v145
	v_and_b32_e32 v51, s27, v145
	v_lshlrev_b32_e32 v52, 16, v146
	v_and_b32_e32 v53, s27, v146
	v_lshlrev_b32_e32 v54, 16, v147
	v_and_b32_e32 v55, s27, v147
	v_lshlrev_b32_e32 v56, 16, v208
	v_and_b32_e32 v57, s27, v208
	v_lshlrev_b32_e32 v58, 16, v209
	v_and_b32_e32 v59, s27, v209
	v_lshlrev_b32_e32 v60, 16, v210
	v_and_b32_e32 v61, s27, v210
	v_lshlrev_b32_e32 v62, 16, v211
	v_and_b32_e32 v63, s27, v211
	v_pk_mul_f32 v[64:65], v[8:9], v[32:33]
	v_pk_mul_f32 v[66:67], v[10:11], v[34:35]
	v_pk_mul_f32 v[68:69], v[12:13], v[36:37]
	v_pk_mul_f32 v[70:71], v[14:15], v[38:39]
	v_pk_fma_f32 v[64:65], v[16:17], v[40:41], v[64:65]
	v_pk_fma_f32 v[66:67], v[18:19], v[42:43], v[66:67]
	v_pk_fma_f32 v[68:69], v[20:21], v[44:45], v[68:69]
	v_pk_fma_f32 v[70:71], v[22:23], v[46:47], v[70:71]
	v_pk_fma_f32 v[64:65], v[24:25], v[48:49], v[64:65]
	v_pk_fma_f32 v[66:67], v[26:27], v[50:51], v[66:67]
	v_pk_fma_f32 v[68:69], v[28:29], v[52:53], v[68:69]
	v_pk_fma_f32 v[70:71], v[30:31], v[54:55], v[70:71]
	v_pk_mul_f32 v[64:65], v[64:65], v[56:57]
	v_pk_mul_f32 v[66:67], v[66:67], v[58:59]
	v_pk_mul_f32 v[68:69], v[68:69], v[60:61]
	v_pk_mul_f32 v[70:71], v[70:71], v[62:63]
	v_cvt_pk_bf16_f32 v72, v64, v65
	v_cvt_pk_bf16_f32 v73, v66, v67
	v_cvt_pk_bf16_f32 v74, v68, v69
	v_cvt_pk_bf16_f32 v75, v70, v71
	global_store_dwordx4 v6, v[72:75], s[14:15]
